# speedup vs baseline: 1.0197x; 1.0107x over previous
.LBB2_3:
	s_lshl_b32 s63, s53, 1
	s_add_i32 s61, s63, 2
	s_sub_i32 s2, s61, s40
	s_lshl_b32 s60, s53, 7
	s_min_i32 s62, s33, s2
	s_cmp_eq_u32 s55, 0
	s_cselect_b32 s79, 0, s62
	s_cmp_lt_i32 s2, 1
	s_cbranch_scc1 .LBB2_21
	s_add_i32 s63, s63, s55
	v_lshl_or_b32 v11, s63, 6, v83
	v_add_u32_e32 v10, s60, v82
	v_or_b32_e32 v12, 2, v11
	v_cmp_gt_i32_e64 s[6:7], v12, v10
	v_or_b32_e32 v12, 3, v11
	v_cmp_gt_i32_e64 s[8:9], v12, v10
	v_or_b32_e32 v12, 16, v11
	v_cmp_gt_i32_e64 s[10:11], v12, v10
	v_or_b32_e32 v12, 17, v11
	v_cmp_gt_i32_e64 s[12:13], v12, v10
	v_or_b32_e32 v12, 18, v11
	v_cmp_gt_i32_e64 s[14:15], v12, v10
	v_or_b32_e32 v12, 19, v11
	v_cmp_gt_i32_e64 s[16:17], v12, v10
	v_or_b32_e32 v12, 32, v11
	v_cmp_gt_i32_e64 s[18:19], v12, v10
	v_or_b32_e32 v12, 33, v11
	v_cmp_gt_i32_e64 s[20:21], v12, v10
	v_or_b32_e32 v12, 34, v11
	v_cmp_gt_i32_e64 s[22:23], v12, v10
	v_or_b32_e32 v12, 35, v11
	v_cmp_gt_i32_e64 s[24:25], v12, v10
	v_or_b32_e32 v12, 48, v11
	s_sub_i32 s37, s56, s40
	v_cmp_gt_i32_e64 s[26:27], v12, v10
	v_or_b32_e32 v12, 49, v11
	s_min_i32 s37, s33, s37
	v_cmp_gt_i32_e64 s[2:3], v11, v10
	v_cmp_lt_i32_e64 s[4:5], v11, v10
	v_cmp_gt_i32_e64 s[28:29], v12, v10
	v_or_b32_e32 v12, 50, v11
	v_or_b32_e32 v11, 51, v11
	s_max_i32 s37, s37, 1
	s_lshl_b64 s[38:39], s[40:41], 13
	v_mov_b32_e32 v67, 0
	v_cmp_gt_i32_e64 s[30:31], v12, v10
	v_cmp_gt_i32_e64 s[34:35], v11, v10
	s_mov_b32 s64, 1
	s_sub_i32 s65, 0, s37
	s_add_i32 s66, s40, s57
	s_add_u32 s68, s70, s38
	s_addc_u32 s69, s71, s39
	s_add_u32 s74, s72, s38
	s_addc_u32 s75, s73, s39
	v_mov_b32_e32 v14, v51
	v_mov_b32_e32 v15, v51
	v_mov_b32_e32 v16, v51
	v_mov_b32_e32 v17, v51
	s_mov_b64 s[38:39], -1
	v_mov_b32_e32 v30, 0
	v_mov_b32_e32 v31, v67
	v_mov_b32_e32 v32, v67
	v_mov_b32_e32 v33, v67
	v_mov_b32_e32 v26, 0
	v_mov_b32_e32 v27, v67
	v_mov_b32_e32 v28, v67
	v_mov_b32_e32 v29, v67
	v_mov_b32_e32 v22, v67
	v_mov_b32_e32 v23, v67
	v_mov_b32_e32 v24, v67
	v_mov_b32_e32 v25, v67
	v_mov_b32_e32 v18, v67
	v_mov_b32_e32 v19, v67
	v_mov_b32_e32 v20, v67
	v_mov_b32_e32 v21, v67
	v_mov_b32_e32 v10, v67
	v_mov_b32_e32 v11, v67
	v_mov_b32_e32 v12, v67
	v_mov_b32_e32 v13, v67
	s_mov_b32 s37, 0
	s_mov_b32 s80, 0
	s_mov_b32 s81, 0
	s_mov_b32 s48, s40
	v_mov_b32_e32 v114, v57
	v_mov_b32_e32 v115, v81
	v_mov_b32_e32 v120, v57
	v_mov_b32_e32 v121, v81
	s_cmp_gt_u32 s48, s63
	s_waitcnt vmcnt(0)
	s_barrier
	s_branch .Lattn_after_rdv

.LBB2_21:
	s_waitcnt vmcnt(0)
	s_barrier
	v_mov_b32_e32 v13, 0
	v_mov_b32_e32 v14, v51
	v_mov_b32_e32 v16, 0xf149f2ca
	v_mov_b32_e32 v12, v13
	v_mov_b32_e32 v11, v13
	v_mov_b32_e32 v10, v13
	v_mov_b32_e32 v21, v13
	v_mov_b32_e32 v20, v13
	v_mov_b32_e32 v19, v13
	v_mov_b32_e32 v18, v13
	v_mov_b32_e32 v25, v13
	v_mov_b32_e32 v24, v13
	v_mov_b32_e32 v23, v13
	v_mov_b32_e32 v22, v13
	v_mov_b32_e32 v29, v13
	v_mov_b32_e32 v28, v13
	v_mov_b32_e32 v27, v13
	v_mov_b32_e32 v26, v13
